# saddr-form K-loops without the 14 placeholder s_nops per loop (loops 1960 B), heads re-aligned to 64B, on top of combo14
# speedup vs baseline: 1.0097x; 1.0007x over previous
; #define PG8_STAGE(bufoff, gbase, voff) do { _Pragma("unroll") for (int _i = 0; _i < 2; ++_i) \
;         __builtin_amdgcn_global_load_lds((const unsigned*)((const char*)(gbase) + (voff)[_i]), (PG8_LAS unsigned*)(lds + (bufoff) + ldsw + _i * 8192), 16, 0, 0); } while (0)
; #define PG8_LDA(dst, b, h) do { _Pragma("unroll") for (int m = 0; m < 4; ++m) _Pragma("unroll") for (int k = 0; k < 2; ++k) dst[m][k] = *(const PG8_LAS bf16x8*)(lds + PG8_SA(b, h) + aoff + m * 2048 + k * 1024); } while (0)
; #define PG8_LDB(dst, b, h) do { _Pragma("unroll") for (int n = 0; n < 2; ++n) _Pragma("unroll") for (int k = 0; k < 2; ++k) dst[n][k] = *(const PG8_LAS bf16x8*)(lds + PG8_SB(b, h) + boff + n * 2048 + k * 1024); } while (0)
; #define PG8_MMA(ai, bj, At, Bt) do { __builtin_amdgcn_s_setprio(1); _Pragma("unroll") for (int m = 0; m < 4; ++m) _Pragma("unroll") for (int n = 0; n < 2; ++n) _Pragma("unroll") for (int k = 0; k < 2; ++k) \
;         acc[ai][bj][m][n] = __builtin_amdgcn_mfma_f32_16x16x32_bf16(Bt[n][k], At[m][k], acc[ai][bj][m][n], 0, 0, 0); __builtin_amdgcn_s_setprio(0); } while (0)
; #define PG8_WAIT_V(n) asm volatile("s_waitcnt vmcnt(" #n ")" ::: "memory")
; #define PG8_WAIT_L(n) asm volatile("s_waitcnt lgkmcnt(" #n ")" ::: "memory")
; template <class Epi, class Sched, bool ALIGN_EPI = false, bool SP2 = false>
; __device__ __forceinline__ void gemm_phase(PG8_LAS unsigned char* lds, const Gemm g, const Sched& S, const Epi& E) {
;     ...
;             const bool last = (t == nt - 2);
;             const char* a1 = cA + (size_t)(t + 1) * kstep;
;             const char* a2 = last ? nA : cA + (size_t)(t + 2) * kstep; const char* b2 = last ? nB : cB + (size_t)(t + 2) * kstep;
;             const char* a3 = a2 + kstep; const char* b3 = b2 + kstep;
;             if (last && has_next) S.a_ready(nxt);
;             if constexpr (SP2) {
;             PG8_LDB(B0, 0, 0); PG8_LDB(B1, 0, 1); PG8_SCHED; PG8_LDA(At, 0, 0); PG8_STAGE(PG8_SA(1, 1), a1 + hstep, voffA);
;             PG8_WAIT_V(8); PG8_WAIT_L(0); PG8_BAR; PG8_MMA(0, 0, At, B0); PG8_MMA(0, 1, At, B1); PG8_BAR; PG8_SCHED;
;             PG8_LDA(At, 0, 1); PG8_STAGE(PG8_SB(0, 0), b2, voffB); PG8_STAGE(PG8_SB(0, 1), b2 + hstep, voffB); PG8_STAGE(PG8_SA(0, 0), a2, voffA);
;             PG8_WAIT_V(8); PG8_WAIT_L(0); PG8_BAR; PG8_MMA(1, 0, At, B0); PG8_MMA(1, 1, At, B1); PG8_BAR; PG8_SCHED;
.LBB0_102:
	ds_read_b128 v[154:157], v159
	ds_read_b128 v[162:165], v159 offset:1024
	ds_read_b128 v[166:169], v159 offset:2048
	ds_read_b128 v[170:173], v159 offset:3072
	ds_read_b128 v[174:177], v160
	ds_read_b128 v[178:181], v160 offset:1024
	ds_read_b128 v[184:187], v160 offset:2048
	ds_read_b128 v[188:191], v160 offset:3072
	s_add_u32 s26, s24, 0xfff00080
	s_addc_u32 s27, s25, -1
	s_cmp_eq_u32 s50, 60
	s_cselect_b32 s29, s17, s27
	s_cselect_b32 s28, s23, s26
	s_cselect_b32 s27, s15, s49
	s_cselect_b32 s26, s46, s47
	s_add_i32 m0, s34, 0xc000
	ds_read_b128 v[192:195], v161
	ds_read_b128 v[196:199], v161 offset:1024
	ds_read_b128 v[200:203], v161 offset:2048
	ds_read_b128 v[204:207], v161 offset:3072
	ds_read_b128 v[208:211], v161 offset:4096
	ds_read_b128 v[212:215], v161 offset:5120
	ds_read_b128 v[216:219], v161 offset:6144
	ds_read_b128 v[220:223], v161 offset:7168
	global_load_lds_dwordx4 v146, s[24:25]
	s_add_i32 m0, s34, 0xe000
	s_nop 0
	global_load_lds_dwordx4 v148, s[24:25]
	s_waitcnt vmcnt(8)
	s_waitcnt lgkmcnt(0)
	s_barrier
	s_setprio 1
	s_waitcnt lgkmcnt(0)
	v_mfma_f32_16x16x32_bf16 v[126:129], v[154:157], v[192:195], v[126:129]
	v_mfma_f32_16x16x32_bf16 v[122:125], v[166:169], v[192:195], v[122:125]
	v_mfma_f32_16x16x32_bf16 v[110:113], v[154:157], v[200:203], v[110:113]
	v_mfma_f32_16x16x32_bf16 v[106:109], v[166:169], v[200:203], v[106:109]
	v_mfma_f32_16x16x32_bf16 v[98:101], v[154:157], v[208:211], v[98:101]
	v_mfma_f32_16x16x32_bf16 v[90:93], v[166:169], v[208:211], v[90:93]
	v_mfma_f32_16x16x32_bf16 v[82:85], v[154:157], v[216:219], v[82:85]
	v_mfma_f32_16x16x32_bf16 v[74:77], v[166:169], v[216:219], v[74:77]
	v_mfma_f32_16x16x32_bf16 v[126:129], v[162:165], v[196:199], v[126:129]
	v_mfma_f32_16x16x32_bf16 v[122:125], v[170:173], v[196:199], v[122:125]
	v_mfma_f32_16x16x32_bf16 v[110:113], v[162:165], v[204:207], v[110:113]
	v_mfma_f32_16x16x32_bf16 v[106:109], v[170:173], v[204:207], v[106:109]
	v_mfma_f32_16x16x32_bf16 v[98:101], v[162:165], v[212:215], v[98:101]
	v_mfma_f32_16x16x32_bf16 v[90:93], v[170:173], v[212:215], v[90:93]
	v_mfma_f32_16x16x32_bf16 v[82:85], v[162:165], v[220:223], v[82:85]
	v_mfma_f32_16x16x32_bf16 v[74:77], v[170:173], v[220:223], v[74:77]
	s_setprio 0
	s_setprio 1
	v_mfma_f32_16x16x32_bf16 v[118:121], v[174:177], v[192:195], v[118:121]
	v_mfma_f32_16x16x32_bf16 v[114:117], v[184:187], v[192:195], v[114:117]
	v_mfma_f32_16x16x32_bf16 v[102:105], v[174:177], v[200:203], v[102:105]
	v_mfma_f32_16x16x32_bf16 v[94:97], v[184:187], v[200:203], v[94:97]
	v_mfma_f32_16x16x32_bf16 v[86:89], v[174:177], v[208:211], v[86:89]
	v_mfma_f32_16x16x32_bf16 v[78:81], v[184:187], v[208:211], v[78:81]
	v_mfma_f32_16x16x32_bf16 v[70:73], v[174:177], v[216:219], v[70:73]
	v_mfma_f32_16x16x32_bf16 v[66:69], v[184:187], v[216:219], v[66:69]
	v_mfma_f32_16x16x32_bf16 v[118:121], v[178:181], v[196:199], v[118:121]
	v_mfma_f32_16x16x32_bf16 v[114:117], v[188:191], v[196:199], v[114:117]
	v_mfma_f32_16x16x32_bf16 v[102:105], v[178:181], v[204:207], v[102:105]
	v_mfma_f32_16x16x32_bf16 v[94:97], v[188:191], v[204:207], v[94:97]
	v_mfma_f32_16x16x32_bf16 v[86:89], v[178:181], v[212:215], v[86:89]
	v_mfma_f32_16x16x32_bf16 v[78:81], v[188:191], v[212:215], v[78:81]
	v_mfma_f32_16x16x32_bf16 v[70:73], v[178:181], v[220:223], v[70:73]
	v_mfma_f32_16x16x32_bf16 v[66:69], v[188:191], v[220:223], v[66:69]
	s_setprio 0
	s_barrier
	s_add_i32 s51, s42, s30
	s_mov_b32 m0, s51
	ds_read_b128 v[192:195], v161 offset:16384
	ds_read_b128 v[196:199], v161 offset:17408
	ds_read_b128 v[200:203], v161 offset:18432
	ds_read_b128 v[204:207], v161 offset:19456
	ds_read_b128 v[208:211], v161 offset:20480
	ds_read_b128 v[212:215], v161 offset:21504
	ds_read_b128 v[216:219], v161 offset:22528
	ds_read_b128 v[220:223], v161 offset:23552
	global_load_lds_dwordx4 v140, s[26:27]
	s_add_i32 m0, s51, 0x2000
	s_add_u32 s52, s26, 0x100000
	s_addc_u32 s53, s27, 0
	s_add_i32 s51, s43, s30
	global_load_lds_dwordx4 v136, s[26:27]
	s_mov_b32 m0, s51
	s_add_u32 s58, s28, s6
	s_addc_u32 s59, s29, s7
	global_load_lds_dwordx4 v140, s[52:53]
	s_add_i32 m0, s51, 0x2000
	s_nop 0
	global_load_lds_dwordx4 v136, s[52:53]
	s_mov_b32 m0, s34
	s_nop 0
	global_load_lds_dwordx4 v142, s[28:29]
	s_mov_b32 m0, s35
	s_nop 0
	global_load_lds_dwordx4 v138, s[28:29]
	s_waitcnt vmcnt(8)
	s_waitcnt lgkmcnt(0)
	s_barrier
	s_setprio 1
	s_waitcnt lgkmcnt(0)
	v_mfma_f32_16x16x32_bf16 v[62:65], v[154:157], v[192:195], v[62:65]
	v_mfma_f32_16x16x32_bf16 v[58:61], v[166:169], v[192:195], v[58:61]
	v_mfma_f32_16x16x32_bf16 v[50:53], v[154:157], v[200:203], v[50:53]
	v_mfma_f32_16x16x32_bf16 v[42:45], v[166:169], v[200:203], v[42:45]
	v_mfma_f32_16x16x32_bf16 v[34:37], v[154:157], v[208:211], v[34:37]
	v_mfma_f32_16x16x32_bf16 v[26:29], v[166:169], v[208:211], v[26:29]
	v_mfma_f32_16x16x32_bf16 v[18:21], v[154:157], v[216:219], v[18:21]
	v_mfma_f32_16x16x32_bf16 v[10:13], v[166:169], v[216:219], v[10:13]
	v_mfma_f32_16x16x32_bf16 v[62:65], v[162:165], v[196:199], v[62:65]
	v_mfma_f32_16x16x32_bf16 v[58:61], v[170:173], v[196:199], v[58:61]
	v_mfma_f32_16x16x32_bf16 v[50:53], v[162:165], v[204:207], v[50:53]
	v_mfma_f32_16x16x32_bf16 v[42:45], v[170:173], v[204:207], v[42:45]
	v_mfma_f32_16x16x32_bf16 v[34:37], v[162:165], v[212:215], v[34:37]
	v_mfma_f32_16x16x32_bf16 v[26:29], v[170:173], v[212:215], v[26:29]
	v_mfma_f32_16x16x32_bf16 v[18:21], v[162:165], v[220:223], v[18:21]
	v_mfma_f32_16x16x32_bf16 v[10:13], v[170:173], v[220:223], v[10:13]
	s_setprio 0
	s_setprio 1
	v_mfma_f32_16x16x32_bf16 v[54:57], v[174:177], v[192:195], v[54:57]
	v_mfma_f32_16x16x32_bf16 v[46:49], v[184:187], v[192:195], v[46:49]
	v_mfma_f32_16x16x32_bf16 v[38:41], v[174:177], v[200:203], v[38:41]
	v_mfma_f32_16x16x32_bf16 v[30:33], v[184:187], v[200:203], v[30:33]
	v_mfma_f32_16x16x32_bf16 v[22:25], v[174:177], v[208:211], v[22:25]
	v_mfma_f32_16x16x32_bf16 v[14:17], v[184:187], v[208:211], v[14:17]
	v_mfma_f32_16x16x32_bf16 v[6:9], v[174:177], v[216:219], v[6:9]
	v_mfma_f32_16x16x32_bf16 v[2:5], v[184:187], v[216:219], v[2:5]
	v_mfma_f32_16x16x32_bf16 v[54:57], v[178:181], v[196:199], v[54:57]
	v_mfma_f32_16x16x32_bf16 v[46:49], v[188:191], v[196:199], v[46:49]
	v_mfma_f32_16x16x32_bf16 v[38:41], v[178:181], v[204:207], v[38:41]
	v_mfma_f32_16x16x32_bf16 v[30:33], v[188:191], v[204:207], v[30:33]
	v_mfma_f32_16x16x32_bf16 v[22:25], v[178:181], v[212:215], v[22:25]
	v_mfma_f32_16x16x32_bf16 v[14:17], v[188:191], v[212:215], v[14:17]
	v_mfma_f32_16x16x32_bf16 v[6:9], v[178:181], v[220:223], v[6:9]
	v_mfma_f32_16x16x32_bf16 v[2:5], v[188:191], v[220:223], v[2:5]
	s_setprio 0
	s_barrier
; #define PG8_STAGE(bufoff, gbase, voff) do { _Pragma("unroll") for (int _i = 0; _i < 2; ++_i) \
;         __builtin_amdgcn_global_load_lds((const unsigned*)((const char*)(gbase) + (voff)[_i]), (PG8_LAS unsigned*)(lds + (bufoff) + ldsw + _i * 8192), 16, 0, 0); } while (0)
; #define PG8_LDA(dst, b, h) do { _Pragma("unroll") for (int m = 0; m < 4; ++m) _Pragma("unroll") for (int k = 0; k < 2; ++k) dst[m][k] = *(const PG8_LAS bf16x8*)(lds + PG8_SA(b, h) + aoff + m * 2048 + k * 1024); } while (0)
; #define PG8_LDB(dst, b, h) do { _Pragma("unroll") for (int n = 0; n < 2; ++n) _Pragma("unroll") for (int k = 0; k < 2; ++k) dst[n][k] = *(const PG8_LAS bf16x8*)(lds + PG8_SB(b, h) + boff + n * 2048 + k * 1024); } while (0)
; #define PG8_MMA(ai, bj, At, Bt) do { __builtin_amdgcn_s_setprio(1); _Pragma("unroll") for (int m = 0; m < 4; ++m) _Pragma("unroll") for (int n = 0; n < 2; ++n) _Pragma("unroll") for (int k = 0; k < 2; ++k) \
;         acc[ai][bj][m][n] = __builtin_amdgcn_mfma_f32_16x16x32_bf16(Bt[n][k], At[m][k], acc[ai][bj][m][n], 0, 0, 0); __builtin_amdgcn_s_setprio(0); } while (0)
; #define PG8_WAIT_V(n) asm volatile("s_waitcnt vmcnt(" #n ")" ::: "memory")
; #define PG8_WAIT_L(n) asm volatile("s_waitcnt lgkmcnt(" #n ")" ::: "memory")
; #define PG8_BAR __builtin_amdgcn_s_barrier()
; #define PG8_SCHED __builtin_amdgcn_sched_barrier(0)
; template <class Epi, class Sched, bool ALIGN_EPI = false, bool SP2 = false>
; __device__ __forceinline__ void gemm_phase(PG8_LAS unsigned char* lds, const Gemm g, const Sched& S, const Epi& E) {
;     ...
;             PG8_LDB(B0, 1, 0); PG8_LDB(B1, 1, 1); PG8_SCHED; PG8_LDA(At, 1, 0); PG8_STAGE(PG8_SA(0, 1), a2 + hstep, voffA);
;             PG8_WAIT_V(8); PG8_WAIT_L(0); PG8_BAR; PG8_MMA(0, 0, At, B0); PG8_MMA(0, 1, At, B1); PG8_BAR; PG8_SCHED;
;             PG8_LDA(At, 1, 1); PG8_STAGE(PG8_SB(1, 0), b3, voffB); PG8_STAGE(PG8_SB(1, 1), b3 + hstep, voffB); PG8_STAGE(PG8_SA(1, 0), a3, voffA);
;             PG8_WAIT_V(8); PG8_WAIT_L(0); PG8_BAR; PG8_MMA(1, 0, At, B0); PG8_MMA(1, 1, At, B1); PG8_BAR; PG8_SCHED;
;     ...
;         if constexpr (ALIGN_EPI) { if (wr == 0) PG8_BAR; }
	s_add_i32 s51, 0, 0x18000
	v_add_u32_e32 v144, s51, v133
	s_add_i32 s52, 0, 0x1c000
	ds_read_b128 v[154:157], v144
	ds_read_b128 v[162:165], v144 offset:1024
	ds_read_b128 v[166:169], v144 offset:2048
	ds_read_b128 v[170:173], v144 offset:3072
	v_add_u32_e32 v144, s52, v133
	ds_read_b128 v[174:177], v144
	ds_read_b128 v[178:181], v144 offset:1024
	ds_read_b128 v[184:187], v144 offset:2048
	ds_read_b128 v[188:191], v144 offset:3072
	s_add_u32 s28, s28, 0x100000
	s_addc_u32 s29, s29, 0
	s_mov_b32 m0, s36
	ds_read_b128 v[192:195], v161 offset:32768
	ds_read_b128 v[196:199], v161 offset:33792
	ds_read_b128 v[200:203], v161 offset:34816
	ds_read_b128 v[204:207], v161 offset:35840
	ds_read_b128 v[208:211], v161 offset:36864
	ds_read_b128 v[212:215], v161 offset:37888
	ds_read_b128 v[216:219], v161 offset:38912
	ds_read_b128 v[220:223], v161 offset:39936
	global_load_lds_dwordx4 v142, s[28:29]
	s_mov_b32 m0, s37
	s_nop 0
	global_load_lds_dwordx4 v138, s[28:29]
	s_waitcnt vmcnt(8)
	s_waitcnt lgkmcnt(0)
	s_barrier
	s_setprio 1
	s_waitcnt lgkmcnt(0)
	v_mfma_f32_16x16x32_bf16 v[126:129], v[154:157], v[192:195], v[126:129]
	v_mfma_f32_16x16x32_bf16 v[122:125], v[166:169], v[192:195], v[122:125]
	v_mfma_f32_16x16x32_bf16 v[110:113], v[154:157], v[200:203], v[110:113]
	v_mfma_f32_16x16x32_bf16 v[106:109], v[166:169], v[200:203], v[106:109]
	v_mfma_f32_16x16x32_bf16 v[98:101], v[154:157], v[208:211], v[98:101]
	v_mfma_f32_16x16x32_bf16 v[90:93], v[166:169], v[208:211], v[90:93]
	v_mfma_f32_16x16x32_bf16 v[82:85], v[154:157], v[216:219], v[82:85]
	v_mfma_f32_16x16x32_bf16 v[74:77], v[166:169], v[216:219], v[74:77]
	v_mfma_f32_16x16x32_bf16 v[126:129], v[162:165], v[196:199], v[126:129]
	v_mfma_f32_16x16x32_bf16 v[122:125], v[170:173], v[196:199], v[122:125]
	v_mfma_f32_16x16x32_bf16 v[110:113], v[162:165], v[204:207], v[110:113]
	v_mfma_f32_16x16x32_bf16 v[106:109], v[170:173], v[204:207], v[106:109]
	v_mfma_f32_16x16x32_bf16 v[98:101], v[162:165], v[212:215], v[98:101]
	v_mfma_f32_16x16x32_bf16 v[90:93], v[170:173], v[212:215], v[90:93]
	v_mfma_f32_16x16x32_bf16 v[82:85], v[162:165], v[220:223], v[82:85]
	v_mfma_f32_16x16x32_bf16 v[74:77], v[170:173], v[220:223], v[74:77]
	s_setprio 0
	s_setprio 1
	v_mfma_f32_16x16x32_bf16 v[118:121], v[174:177], v[192:195], v[118:121]
	v_mfma_f32_16x16x32_bf16 v[114:117], v[184:187], v[192:195], v[114:117]
	v_mfma_f32_16x16x32_bf16 v[102:105], v[174:177], v[200:203], v[102:105]
	v_mfma_f32_16x16x32_bf16 v[94:97], v[184:187], v[200:203], v[94:97]
	v_mfma_f32_16x16x32_bf16 v[86:89], v[174:177], v[208:211], v[86:89]
	v_mfma_f32_16x16x32_bf16 v[78:81], v[184:187], v[208:211], v[78:81]
	v_mfma_f32_16x16x32_bf16 v[70:73], v[174:177], v[216:219], v[70:73]
	v_mfma_f32_16x16x32_bf16 v[66:69], v[184:187], v[216:219], v[66:69]
	v_mfma_f32_16x16x32_bf16 v[118:121], v[178:181], v[196:199], v[118:121]
	v_mfma_f32_16x16x32_bf16 v[114:117], v[188:191], v[196:199], v[114:117]
	v_mfma_f32_16x16x32_bf16 v[102:105], v[178:181], v[204:207], v[102:105]
	v_mfma_f32_16x16x32_bf16 v[94:97], v[188:191], v[204:207], v[94:97]
	v_mfma_f32_16x16x32_bf16 v[86:89], v[178:181], v[212:215], v[86:89]
	v_mfma_f32_16x16x32_bf16 v[78:81], v[188:191], v[212:215], v[78:81]
	v_mfma_f32_16x16x32_bf16 v[70:73], v[178:181], v[220:223], v[70:73]
	v_mfma_f32_16x16x32_bf16 v[66:69], v[188:191], v[220:223], v[66:69]
	s_setprio 0
	s_barrier
	s_add_i32 s28, s51, s30
	s_add_u32 s54, s26, s6
	s_addc_u32 s55, s27, s7
	s_mov_b32 m0, s28
	ds_read_b128 v[192:195], v161 offset:49152
	ds_read_b128 v[196:199], v161 offset:50176
	ds_read_b128 v[200:203], v161 offset:51200
	ds_read_b128 v[204:207], v161 offset:52224
	ds_read_b128 v[208:211], v161 offset:53248
	ds_read_b128 v[212:215], v161 offset:54272
	ds_read_b128 v[216:219], v161 offset:55296
	ds_read_b128 v[220:223], v161 offset:56320
	global_load_lds_dwordx4 v140, s[54:55]
	s_add_i32 m0, s28, 0x2000
	s_add_u32 s26, s26, 0x100080
	s_addc_u32 s27, s27, 0
	s_add_i32 s28, s52, s30
	global_load_lds_dwordx4 v136, s[54:55]
	s_mov_b32 m0, s28
	s_nop 0
	global_load_lds_dwordx4 v140, s[26:27]
	s_add_i32 m0, s28, 0x2000
	s_nop 0
	global_load_lds_dwordx4 v136, s[26:27]
	s_mov_b32 m0, s39
	s_nop 0
	global_load_lds_dwordx4 v142, s[58:59]
	s_mov_b32 m0, s40
	s_nop 0
	global_load_lds_dwordx4 v138, s[58:59]
	s_waitcnt vmcnt(8)
	s_waitcnt lgkmcnt(0)
	s_barrier
	s_setprio 1
	s_waitcnt lgkmcnt(0)
	v_mfma_f32_16x16x32_bf16 v[62:65], v[154:157], v[192:195], v[62:65]
	v_mfma_f32_16x16x32_bf16 v[58:61], v[166:169], v[192:195], v[58:61]
	v_mfma_f32_16x16x32_bf16 v[50:53], v[154:157], v[200:203], v[50:53]
	v_mfma_f32_16x16x32_bf16 v[42:45], v[166:169], v[200:203], v[42:45]
	v_mfma_f32_16x16x32_bf16 v[34:37], v[154:157], v[208:211], v[34:37]
	v_mfma_f32_16x16x32_bf16 v[26:29], v[166:169], v[208:211], v[26:29]
	v_mfma_f32_16x16x32_bf16 v[18:21], v[154:157], v[216:219], v[18:21]
	v_mfma_f32_16x16x32_bf16 v[10:13], v[166:169], v[216:219], v[10:13]
	v_mfma_f32_16x16x32_bf16 v[62:65], v[162:165], v[196:199], v[62:65]
	v_mfma_f32_16x16x32_bf16 v[58:61], v[170:173], v[196:199], v[58:61]
	v_mfma_f32_16x16x32_bf16 v[50:53], v[162:165], v[204:207], v[50:53]
	v_mfma_f32_16x16x32_bf16 v[42:45], v[170:173], v[204:207], v[42:45]
	v_mfma_f32_16x16x32_bf16 v[34:37], v[162:165], v[212:215], v[34:37]
	v_mfma_f32_16x16x32_bf16 v[26:29], v[170:173], v[212:215], v[26:29]
	v_mfma_f32_16x16x32_bf16 v[18:21], v[162:165], v[220:223], v[18:21]
	v_mfma_f32_16x16x32_bf16 v[10:13], v[170:173], v[220:223], v[10:13]
	s_setprio 0
	s_setprio 1
	v_mfma_f32_16x16x32_bf16 v[54:57], v[174:177], v[192:195], v[54:57]
	v_mfma_f32_16x16x32_bf16 v[46:49], v[184:187], v[192:195], v[46:49]
	v_mfma_f32_16x16x32_bf16 v[38:41], v[174:177], v[200:203], v[38:41]
	v_mfma_f32_16x16x32_bf16 v[30:33], v[184:187], v[200:203], v[30:33]
	v_mfma_f32_16x16x32_bf16 v[22:25], v[174:177], v[208:211], v[22:25]
	v_mfma_f32_16x16x32_bf16 v[14:17], v[184:187], v[208:211], v[14:17]
	v_mfma_f32_16x16x32_bf16 v[6:9], v[174:177], v[216:219], v[6:9]
	v_mfma_f32_16x16x32_bf16 v[2:5], v[184:187], v[216:219], v[2:5]
	v_mfma_f32_16x16x32_bf16 v[54:57], v[178:181], v[196:199], v[54:57]
	v_mfma_f32_16x16x32_bf16 v[46:49], v[188:191], v[196:199], v[46:49]
	v_mfma_f32_16x16x32_bf16 v[38:41], v[178:181], v[204:207], v[38:41]
	v_mfma_f32_16x16x32_bf16 v[30:33], v[188:191], v[204:207], v[30:33]
	v_mfma_f32_16x16x32_bf16 v[22:25], v[178:181], v[212:215], v[22:25]
	v_mfma_f32_16x16x32_bf16 v[14:17], v[188:191], v[212:215], v[14:17]
	v_mfma_f32_16x16x32_bf16 v[6:9], v[178:181], v[220:223], v[6:9]
	v_mfma_f32_16x16x32_bf16 v[2:5], v[188:191], v[220:223], v[2:5]
	s_setprio 0
	s_barrier
	s_add_i32 s50, s50, 2
	s_add_u32 s24, s24, 0x100
	s_addc_u32 s25, s25, 0
	s_add_u32 s47, s47, 0x100
	s_addc_u32 s49, s49, 0
	s_cmp_gt_u32 s50, 61
	s_cbranch_scc0 .LBB0_102
	s_and_b64 vcc, exec, s[12:13]
	s_cbranch_vccz .LBB0_105
	s_barrier

; #define PG8_STAGE(bufoff, gbase, voff) do { _Pragma("unroll") for (int _i = 0; _i < 2; ++_i) \
;         __builtin_amdgcn_global_load_lds((const unsigned*)((const char*)(gbase) + (voff)[_i]), (PG8_LAS unsigned*)(lds + (bufoff) + ldsw + _i * 8192), 16, 0, 0); } while (0)
; #define PG8_LDA(dst, b, h) do { _Pragma("unroll") for (int m = 0; m < 4; ++m) _Pragma("unroll") for (int k = 0; k < 2; ++k) dst[m][k] = *(const PG8_LAS bf16x8*)(lds + PG8_SA(b, h) + aoff + m * 2048 + k * 1024); } while (0)
; #define PG8_LDB(dst, b, h) do { _Pragma("unroll") for (int n = 0; n < 2; ++n) _Pragma("unroll") for (int k = 0; k < 2; ++k) dst[n][k] = *(const PG8_LAS bf16x8*)(lds + PG8_SB(b, h) + boff + n * 2048 + k * 1024); } while (0)
; #define PG8_WAIT_V(n) asm volatile("s_waitcnt vmcnt(" #n ")" ::: "memory")
; #define PG8_WAIT_L(n) asm volatile("s_waitcnt lgkmcnt(" #n ")" ::: "memory")
; #define PG8_BAR __builtin_amdgcn_s_barrier()
; template <class Epi, class Sched, bool ALIGN_EPI = false, bool SP2 = false>
; __device__ __forceinline__ void gemm_phase(PG8_LAS unsigned char* lds, const Gemm g, const Sched& S, const Epi& E) {
;     ...
;         const bool has_next = S.next(ui + 1, nxt);
;         const char* nA = has_next ? (const char*)g.A + (size_t)nxt.pm * tstep : cA; const char* nB = has_next ? (const char*)g.Bt + (size_t)nxt.pn * tstep : cB;
;         for (int t = 0; t < nt; t += 2) {
;             const bool last = (t == nt - 2);
;             const char* a1 = cA + (size_t)(t + 1) * kstep;
;             const char* a2 = last ? nA : cA + (size_t)(t + 2) * kstep; const char* b2 = last ? nB : cB + (size_t)(t + 2) * kstep;
;             const char* a3 = a2 + kstep; const char* b3 = b2 + kstep;
;             if (last && has_next) S.a_ready(nxt);
;             if constexpr (SP2) {
;             PG8_LDB(B0, 0, 0); PG8_LDB(B1, 0, 1); PG8_SCHED; PG8_LDA(At, 0, 0); PG8_STAGE(PG8_SA(1, 1), a1 + hstep, voffA);
;             PG8_WAIT_V(8); PG8_WAIT_L(0); PG8_BAR; PG8_MMA(0, 0, At, B0); PG8_MMA(0, 1, At, B1); PG8_BAR; PG8_SCHED;
;     ...
; #pragma unroll
;         for (int a = 0; a < 2; ++a)
; #pragma unroll
;             for (int b = 0; b < 2; ++b)
; #pragma unroll
;                 for (int m = 0; m < 4; ++m)
; #pragma unroll
;                     for (int n = 0; n < 2; ++n) acc[a][b][m][n] = (f32x4){0.f, 0.f, 0.f, 0.f};
;         cur = nxt; cA = nA; cB = nB; ++ui;
.LBB0_562:
	s_ashr_i32 s21, s20, 31
	s_lshl_b64 s[22:23], s[20:21], 22
	s_add_u32 s22, s64, s22
	s_addc_u32 s23, s65, s23
	s_and_b64 s[24:25], s[4:5], exec
	s_cselect_b32 s21, s23, s29
	s_cselect_b32 s47, s22, s28
	s_ashr_i32 s19, s18, 31
	s_lshl_b64 s[24:25], s[18:19], 22
	s_add_u32 s24, s56, s24
	s_addc_u32 s25, s57, s25
	s_and_b64 s[34:35], s[4:5], exec
	s_cselect_b32 s19, s25, s31
	s_cselect_b32 s48, s24, s30
	s_add_u32 s28, s28, 0x200080
	s_addc_u32 s29, s29, 0
	s_add_u32 s49, s30, 0x100
	v_mov_b32_e32 v2, 0
	s_addc_u32 s50, s31, 0
	s_mov_b32 s51, -2
	v_mov_b32_e32 v3, v2
	v_mov_b32_e32 v4, v2
	v_mov_b32_e32 v5, v2
	v_mov_b32_e32 v6, v2
	v_mov_b32_e32 v7, v2
	v_mov_b32_e32 v8, v2
	v_mov_b32_e32 v9, v2
	v_mov_b32_e32 v18, v2
	v_mov_b32_e32 v19, v2
	v_mov_b32_e32 v20, v2
	v_mov_b32_e32 v21, v2
	v_mov_b32_e32 v22, v2
	v_mov_b32_e32 v23, v2
	v_mov_b32_e32 v24, v2
	v_mov_b32_e32 v25, v2
	v_mov_b32_e32 v34, v2
	v_mov_b32_e32 v35, v2
	v_mov_b32_e32 v36, v2
	v_mov_b32_e32 v37, v2
	v_mov_b32_e32 v38, v2
	v_mov_b32_e32 v39, v2
	v_mov_b32_e32 v40, v2
	v_mov_b32_e32 v41, v2
	v_mov_b32_e32 v50, v2
	v_mov_b32_e32 v51, v2
	v_mov_b32_e32 v52, v2
	v_mov_b32_e32 v53, v2
	v_mov_b32_e32 v54, v2
	v_mov_b32_e32 v55, v2
	v_mov_b32_e32 v56, v2
	v_mov_b32_e32 v57, v2
	v_mov_b32_e32 v10, v2
	v_mov_b32_e32 v11, v2
	v_mov_b32_e32 v12, v2
	v_mov_b32_e32 v13, v2
	v_mov_b32_e32 v14, v2
	v_mov_b32_e32 v15, v2
	v_mov_b32_e32 v16, v2
	v_mov_b32_e32 v17, v2
	v_mov_b32_e32 v26, v2
	v_mov_b32_e32 v27, v2
	v_mov_b32_e32 v28, v2
	v_mov_b32_e32 v29, v2
	v_mov_b32_e32 v30, v2
	v_mov_b32_e32 v31, v2
	v_mov_b32_e32 v32, v2
	v_mov_b32_e32 v33, v2
	v_mov_b32_e32 v42, v2
	v_mov_b32_e32 v43, v2
	v_mov_b32_e32 v44, v2
	v_mov_b32_e32 v45, v2
	v_mov_b32_e32 v46, v2
	v_mov_b32_e32 v47, v2
	v_mov_b32_e32 v48, v2
	v_mov_b32_e32 v49, v2
	v_mov_b32_e32 v58, v2
	v_mov_b32_e32 v59, v2
	v_mov_b32_e32 v60, v2
	v_mov_b32_e32 v61, v2
	v_mov_b32_e32 v62, v2
	v_mov_b32_e32 v63, v2
	v_mov_b32_e32 v64, v2
	v_mov_b32_e32 v65, v2
	s_waitcnt vmcnt(0)
	v_mov_b32_e32 v66, v2
	v_mov_b32_e32 v67, v2
	v_mov_b32_e32 v68, v2
	v_mov_b32_e32 v69, v2
	v_mov_b32_e32 v70, v2
	v_mov_b32_e32 v71, v2
	v_mov_b32_e32 v72, v2
	v_mov_b32_e32 v73, v2
	v_mov_b32_e32 v82, v2
	v_mov_b32_e32 v83, v2
	v_mov_b32_e32 v84, v2
	v_mov_b32_e32 v85, v2
	v_mov_b32_e32 v86, v2
	v_mov_b32_e32 v87, v2
	v_mov_b32_e32 v88, v2
	v_mov_b32_e32 v89, v2
	v_mov_b32_e32 v98, v2
	v_mov_b32_e32 v99, v2
	v_mov_b32_e32 v100, v2
	v_mov_b32_e32 v101, v2
	v_mov_b32_e32 v102, v2
	v_mov_b32_e32 v103, v2
	v_mov_b32_e32 v104, v2
	v_mov_b32_e32 v105, v2
	v_mov_b32_e32 v114, v2
	v_mov_b32_e32 v115, v2
	v_mov_b32_e32 v116, v2
	v_mov_b32_e32 v117, v2
	v_mov_b32_e32 v118, v2
	v_mov_b32_e32 v119, v2
	v_mov_b32_e32 v120, v2
	v_mov_b32_e32 v121, v2
	v_mov_b32_e32 v74, v2
	v_mov_b32_e32 v75, v2
	v_mov_b32_e32 v76, v2
	v_mov_b32_e32 v77, v2
	v_mov_b32_e32 v78, v2
	v_mov_b32_e32 v79, v2
	v_mov_b32_e32 v80, v2
	v_mov_b32_e32 v81, v2
	v_mov_b32_e32 v90, v2
	v_mov_b32_e32 v91, v2
	v_mov_b32_e32 v92, v2
	v_mov_b32_e32 v93, v2
	v_mov_b32_e32 v94, v2
	v_mov_b32_e32 v95, v2
	v_mov_b32_e32 v96, v2
	v_mov_b32_e32 v97, v2
	v_mov_b32_e32 v106, v2
	v_mov_b32_e32 v107, v2
	v_mov_b32_e32 v108, v2
	v_mov_b32_e32 v109, v2
	v_mov_b32_e32 v110, v2
	v_mov_b32_e32 v111, v2
	v_mov_b32_e32 v112, v2
	v_mov_b32_e32 v113, v2
	v_mov_b32_e32 v122, v2
	v_mov_b32_e32 v123, v2
	v_mov_b32_e32 v124, v2
	v_mov_b32_e32 v125, v2
	v_mov_b32_e32 v126, v2
	v_mov_b32_e32 v127, v2
	v_mov_b32_e32 v128, v2
	v_mov_b32_e32 v129, v2
	s_nop 0
	s_nop 0
	s_nop 0
	s_nop 0
	s_nop 0
	s_nop 0
	s_nop 0
	s_nop 0
	s_nop 0
	s_nop 0
	s_nop 0
	s_nop 0
	s_nop 0
	s_nop 0
	s_nop 0
.LBB0_563:
	ds_read_b128 v[146:149], v154
	ds_read_b128 v[158:161], v154 offset:1024
	ds_read_b128 v[162:165], v154 offset:2048
	ds_read_b128 v[166:169], v154 offset:3072
	ds_read_b128 v[170:173], v155
	ds_read_b128 v[174:177], v155 offset:1024
	ds_read_b128 v[178:181], v155 offset:2048
	ds_read_b128 v[184:187], v155 offset:3072
	s_add_u32 s30, s28, 0xffe00080
	s_addc_u32 s31, s29, -1
	s_cmpk_eq_i32 s51, 0x7c
	s_cselect_b32 s35, s21, s31
	s_cselect_b32 s34, s47, s30
	s_cselect_b32 s31, s19, s50
	s_cselect_b32 s30, s48, s49
	s_add_i32 m0, s27, 0xc000
	ds_read_b128 v[188:191], v156
	ds_read_b128 v[192:195], v156 offset:1024
	ds_read_b128 v[196:199], v156 offset:2048
	ds_read_b128 v[200:203], v156 offset:3072
	ds_read_b128 v[204:207], v156 offset:4096
	ds_read_b128 v[208:211], v156 offset:5120
	ds_read_b128 v[212:215], v156 offset:6144
	ds_read_b128 v[216:219], v156 offset:7168
	global_load_lds_dwordx4 v138, s[28:29]
	s_add_i32 m0, s27, 0xe000
	s_nop 0
	global_load_lds_dwordx4 v140, s[28:29]
	s_waitcnt vmcnt(8)
	s_waitcnt lgkmcnt(0)
	s_barrier
; #define PG8_STAGE(bufoff, gbase, voff) do { _Pragma("unroll") for (int _i = 0; _i < 2; ++_i) \
;         __builtin_amdgcn_global_load_lds((const unsigned*)((const char*)(gbase) + (voff)[_i]), (PG8_LAS unsigned*)(lds + (bufoff) + ldsw + _i * 8192), 16, 0, 0); } while (0)
; #define PG8_LDA(dst, b, h) do { _Pragma("unroll") for (int m = 0; m < 4; ++m) _Pragma("unroll") for (int k = 0; k < 2; ++k) dst[m][k] = *(const PG8_LAS bf16x8*)(lds + PG8_SA(b, h) + aoff + m * 2048 + k * 1024); } while (0)
; #define PG8_MMA(ai, bj, At, Bt) do { __builtin_amdgcn_s_setprio(1); _Pragma("unroll") for (int m = 0; m < 4; ++m) _Pragma("unroll") for (int n = 0; n < 2; ++n) _Pragma("unroll") for (int k = 0; k < 2; ++k) \
;         acc[ai][bj][m][n] = __builtin_amdgcn_mfma_f32_16x16x32_bf16(Bt[n][k], At[m][k], acc[ai][bj][m][n], 0, 0, 0); __builtin_amdgcn_s_setprio(0); } while (0)
; #define PG8_WAIT_V(n) asm volatile("s_waitcnt vmcnt(" #n ")" ::: "memory")
; #define PG8_WAIT_L(n) asm volatile("s_waitcnt lgkmcnt(" #n ")" ::: "memory")
; #define PG8_BAR __builtin_amdgcn_s_barrier()
; #define PG8_SCHED __builtin_amdgcn_sched_barrier(0)
; template <class Epi, class Sched, bool ALIGN_EPI = false, bool SP2 = false>
; __device__ __forceinline__ void gemm_phase(PG8_LAS unsigned char* lds, const Gemm g, const Sched& S, const Epi& E) {
;     ...
;             PG8_WAIT_V(8); PG8_WAIT_L(0); PG8_BAR; PG8_MMA(0, 0, At, B0); PG8_MMA(0, 1, At, B1); PG8_BAR; PG8_SCHED;
;             PG8_LDA(At, 0, 1); PG8_STAGE(PG8_SB(0, 0), b2, voffB); PG8_STAGE(PG8_SB(0, 1), b2 + hstep, voffB); PG8_STAGE(PG8_SA(0, 0), a2, voffA);
;             PG8_WAIT_V(8); PG8_WAIT_L(0); PG8_BAR; PG8_MMA(1, 0, At, B0); PG8_MMA(1, 1, At, B1); PG8_BAR; PG8_SCHED;
	s_setprio 1
	s_waitcnt lgkmcnt(0)
	v_mfma_f32_16x16x32_bf16 v[126:129], v[146:149], v[188:191], v[126:129]
	v_mfma_f32_16x16x32_bf16 v[122:125], v[162:165], v[188:191], v[122:125]
	v_mfma_f32_16x16x32_bf16 v[110:113], v[146:149], v[196:199], v[110:113]
	v_mfma_f32_16x16x32_bf16 v[106:109], v[162:165], v[196:199], v[106:109]
	v_mfma_f32_16x16x32_bf16 v[94:97], v[146:149], v[204:207], v[94:97]
	v_mfma_f32_16x16x32_bf16 v[90:93], v[162:165], v[204:207], v[90:93]
	v_mfma_f32_16x16x32_bf16 v[78:81], v[146:149], v[212:215], v[78:81]
	v_mfma_f32_16x16x32_bf16 v[74:77], v[162:165], v[212:215], v[74:77]
	v_mfma_f32_16x16x32_bf16 v[126:129], v[158:161], v[192:195], v[126:129]
	v_mfma_f32_16x16x32_bf16 v[122:125], v[166:169], v[192:195], v[122:125]
	v_mfma_f32_16x16x32_bf16 v[110:113], v[158:161], v[200:203], v[110:113]
	v_mfma_f32_16x16x32_bf16 v[106:109], v[166:169], v[200:203], v[106:109]
	v_mfma_f32_16x16x32_bf16 v[94:97], v[158:161], v[208:211], v[94:97]
	v_mfma_f32_16x16x32_bf16 v[90:93], v[166:169], v[208:211], v[90:93]
	v_mfma_f32_16x16x32_bf16 v[78:81], v[158:161], v[216:219], v[78:81]
	v_mfma_f32_16x16x32_bf16 v[74:77], v[166:169], v[216:219], v[74:77]
	s_setprio 0
	s_setprio 1
	v_mfma_f32_16x16x32_bf16 v[118:121], v[170:173], v[188:191], v[118:121]
	v_mfma_f32_16x16x32_bf16 v[114:117], v[178:181], v[188:191], v[114:117]
	v_mfma_f32_16x16x32_bf16 v[102:105], v[170:173], v[196:199], v[102:105]
	v_mfma_f32_16x16x32_bf16 v[98:101], v[178:181], v[196:199], v[98:101]
	v_mfma_f32_16x16x32_bf16 v[86:89], v[170:173], v[204:207], v[86:89]
	v_mfma_f32_16x16x32_bf16 v[82:85], v[178:181], v[204:207], v[82:85]
	v_mfma_f32_16x16x32_bf16 v[70:73], v[170:173], v[212:215], v[70:73]
	v_mfma_f32_16x16x32_bf16 v[66:69], v[178:181], v[212:215], v[66:69]
	v_mfma_f32_16x16x32_bf16 v[118:121], v[174:177], v[192:195], v[118:121]
	v_mfma_f32_16x16x32_bf16 v[114:117], v[184:187], v[192:195], v[114:117]
	v_mfma_f32_16x16x32_bf16 v[102:105], v[174:177], v[200:203], v[102:105]
	v_mfma_f32_16x16x32_bf16 v[98:101], v[184:187], v[200:203], v[98:101]
	v_mfma_f32_16x16x32_bf16 v[86:89], v[174:177], v[208:211], v[86:89]
	v_mfma_f32_16x16x32_bf16 v[82:85], v[184:187], v[208:211], v[82:85]
	v_mfma_f32_16x16x32_bf16 v[70:73], v[174:177], v[216:219], v[70:73]
	v_mfma_f32_16x16x32_bf16 v[66:69], v[184:187], v[216:219], v[66:69]
	s_setprio 0
	s_barrier
	s_add_i32 s52, s44, s36
	s_mov_b32 m0, s52
	ds_read_b128 v[188:191], v156 offset:16384
	ds_read_b128 v[192:195], v156 offset:17408
	ds_read_b128 v[196:199], v156 offset:18432
	ds_read_b128 v[200:203], v156 offset:19456
	ds_read_b128 v[204:207], v156 offset:20480
	ds_read_b128 v[208:211], v156 offset:21504
	ds_read_b128 v[212:215], v156 offset:22528
	ds_read_b128 v[216:219], v156 offset:23552
	global_load_lds_dwordx4 v132, s[30:31]
	s_add_i32 m0, s52, 0x2000
	s_add_u32 s52, s30, 0x200000
	s_addc_u32 s53, s31, 0
	s_add_i32 s54, s45, s36
	global_load_lds_dwordx4 v136, s[30:31]
	s_mov_b32 m0, s54
	s_add_u32 s60, s34, s2
	s_addc_u32 s61, s35, s3
	global_load_lds_dwordx4 v132, s[52:53]
	s_add_i32 m0, s54, 0x2000
	s_nop 0
	global_load_lds_dwordx4 v136, s[52:53]
	s_mov_b32 m0, s27
	s_nop 0
	global_load_lds_dwordx4 v130, s[34:35]
	s_mov_b32 m0, s37
	s_nop 0
	global_load_lds_dwordx4 v134, s[34:35]
	s_waitcnt vmcnt(8)
	s_waitcnt lgkmcnt(0)
	s_barrier
	s_setprio 1
	s_waitcnt lgkmcnt(0)
	v_mfma_f32_16x16x32_bf16 v[62:65], v[146:149], v[188:191], v[62:65]
	v_mfma_f32_16x16x32_bf16 v[58:61], v[162:165], v[188:191], v[58:61]
	v_mfma_f32_16x16x32_bf16 v[46:49], v[146:149], v[196:199], v[46:49]
	v_mfma_f32_16x16x32_bf16 v[42:45], v[162:165], v[196:199], v[42:45]
	v_mfma_f32_16x16x32_bf16 v[30:33], v[146:149], v[204:207], v[30:33]
	v_mfma_f32_16x16x32_bf16 v[26:29], v[162:165], v[204:207], v[26:29]
	v_mfma_f32_16x16x32_bf16 v[14:17], v[146:149], v[212:215], v[14:17]
	v_mfma_f32_16x16x32_bf16 v[10:13], v[162:165], v[212:215], v[10:13]
	v_mfma_f32_16x16x32_bf16 v[62:65], v[158:161], v[192:195], v[62:65]
	v_mfma_f32_16x16x32_bf16 v[58:61], v[166:169], v[192:195], v[58:61]
	v_mfma_f32_16x16x32_bf16 v[46:49], v[158:161], v[200:203], v[46:49]
	v_mfma_f32_16x16x32_bf16 v[42:45], v[166:169], v[200:203], v[42:45]
	v_mfma_f32_16x16x32_bf16 v[30:33], v[158:161], v[208:211], v[30:33]
	v_mfma_f32_16x16x32_bf16 v[26:29], v[166:169], v[208:211], v[26:29]
	v_mfma_f32_16x16x32_bf16 v[14:17], v[158:161], v[216:219], v[14:17]
	v_mfma_f32_16x16x32_bf16 v[10:13], v[166:169], v[216:219], v[10:13]
	s_setprio 0
	s_setprio 1
	v_mfma_f32_16x16x32_bf16 v[54:57], v[170:173], v[188:191], v[54:57]
	v_mfma_f32_16x16x32_bf16 v[50:53], v[178:181], v[188:191], v[50:53]
	v_mfma_f32_16x16x32_bf16 v[38:41], v[170:173], v[196:199], v[38:41]
	v_mfma_f32_16x16x32_bf16 v[34:37], v[178:181], v[196:199], v[34:37]
	v_mfma_f32_16x16x32_bf16 v[22:25], v[170:173], v[204:207], v[22:25]
	v_mfma_f32_16x16x32_bf16 v[18:21], v[178:181], v[204:207], v[18:21]
	v_mfma_f32_16x16x32_bf16 v[6:9], v[170:173], v[212:215], v[6:9]
	v_mfma_f32_16x16x32_bf16 v[2:5], v[178:181], v[212:215], v[2:5]
	v_mfma_f32_16x16x32_bf16 v[54:57], v[174:177], v[192:195], v[54:57]
	v_mfma_f32_16x16x32_bf16 v[50:53], v[184:187], v[192:195], v[50:53]
	v_mfma_f32_16x16x32_bf16 v[38:41], v[174:177], v[200:203], v[38:41]
	v_mfma_f32_16x16x32_bf16 v[34:37], v[184:187], v[200:203], v[34:37]
	v_mfma_f32_16x16x32_bf16 v[22:25], v[174:177], v[208:211], v[22:25]
	v_mfma_f32_16x16x32_bf16 v[18:21], v[184:187], v[208:211], v[18:21]
	v_mfma_f32_16x16x32_bf16 v[6:9], v[174:177], v[216:219], v[6:9]
	v_mfma_f32_16x16x32_bf16 v[2:5], v[184:187], v[216:219], v[2:5]
	s_setprio 0
	s_barrier
; #define PG8_STAGE(bufoff, gbase, voff) do { _Pragma("unroll") for (int _i = 0; _i < 2; ++_i) \
;         __builtin_amdgcn_global_load_lds((const unsigned*)((const char*)(gbase) + (voff)[_i]), (PG8_LAS unsigned*)(lds + (bufoff) + ldsw + _i * 8192), 16, 0, 0); } while (0)
; #define PG8_LDA(dst, b, h) do { _Pragma("unroll") for (int m = 0; m < 4; ++m) _Pragma("unroll") for (int k = 0; k < 2; ++k) dst[m][k] = *(const PG8_LAS bf16x8*)(lds + PG8_SA(b, h) + aoff + m * 2048 + k * 1024); } while (0)
; #define PG8_LDB(dst, b, h) do { _Pragma("unroll") for (int n = 0; n < 2; ++n) _Pragma("unroll") for (int k = 0; k < 2; ++k) dst[n][k] = *(const PG8_LAS bf16x8*)(lds + PG8_SB(b, h) + boff + n * 2048 + k * 1024); } while (0)
; #define PG8_MMA(ai, bj, At, Bt) do { __builtin_amdgcn_s_setprio(1); _Pragma("unroll") for (int m = 0; m < 4; ++m) _Pragma("unroll") for (int n = 0; n < 2; ++n) _Pragma("unroll") for (int k = 0; k < 2; ++k) \
;         acc[ai][bj][m][n] = __builtin_amdgcn_mfma_f32_16x16x32_bf16(Bt[n][k], At[m][k], acc[ai][bj][m][n], 0, 0, 0); __builtin_amdgcn_s_setprio(0); } while (0)
; #define PG8_WAIT_V(n) asm volatile("s_waitcnt vmcnt(" #n ")" ::: "memory")
; #define PG8_WAIT_L(n) asm volatile("s_waitcnt lgkmcnt(" #n ")" ::: "memory")
; #define PG8_BAR __builtin_amdgcn_s_barrier()
; #define PG8_SCHED __builtin_amdgcn_sched_barrier(0)
; template <class Epi, class Sched, bool ALIGN_EPI = false, bool SP2 = false>
; __device__ __forceinline__ void gemm_phase(PG8_LAS unsigned char* lds, const Gemm g, const Sched& S, const Epi& E) {
;     ...
;             PG8_LDB(B0, 1, 0); PG8_LDB(B1, 1, 1); PG8_SCHED; PG8_LDA(At, 1, 0); PG8_STAGE(PG8_SA(0, 1), a2 + hstep, voffA);
;             PG8_WAIT_V(8); PG8_WAIT_L(0); PG8_BAR; PG8_MMA(0, 0, At, B0); PG8_MMA(0, 1, At, B1); PG8_BAR; PG8_SCHED;
;             PG8_LDA(At, 1, 1); PG8_STAGE(PG8_SB(1, 0), b3, voffB); PG8_STAGE(PG8_SB(1, 1), b3 + hstep, voffB); PG8_STAGE(PG8_SA(1, 0), a3, voffA);
;             PG8_WAIT_V(8); PG8_WAIT_L(0); PG8_BAR; PG8_MMA(1, 0, At, B0); PG8_MMA(1, 1, At, B1); PG8_BAR; PG8_SCHED;
;     ...
;         if constexpr (ALIGN_EPI) { if (wr == 0) PG8_BAR; }
	s_add_i32 s52, 0, 0x18000
	v_add_u32_e32 v157, s52, v152
	s_add_i32 s53, 0, 0x1c000
	ds_read_b128 v[146:149], v157
	ds_read_b128 v[158:161], v157 offset:1024
	ds_read_b128 v[162:165], v157 offset:2048
	ds_read_b128 v[166:169], v157 offset:3072
	v_add_u32_e32 v157, s53, v152
	ds_read_b128 v[170:173], v157
	ds_read_b128 v[174:177], v157 offset:1024
	ds_read_b128 v[178:181], v157 offset:2048
	ds_read_b128 v[184:187], v157 offset:3072
	s_add_u32 s34, s34, 0x200000
	s_addc_u32 s35, s35, 0
	s_mov_b32 m0, s38
	ds_read_b128 v[188:191], v156 offset:32768
	ds_read_b128 v[192:195], v156 offset:33792
	ds_read_b128 v[196:199], v156 offset:34816
	ds_read_b128 v[200:203], v156 offset:35840
	ds_read_b128 v[204:207], v156 offset:36864
	ds_read_b128 v[208:211], v156 offset:37888
	ds_read_b128 v[212:215], v156 offset:38912
	ds_read_b128 v[216:219], v156 offset:39936
	global_load_lds_dwordx4 v130, s[34:35]
	s_mov_b32 m0, s39
	s_nop 0
	global_load_lds_dwordx4 v134, s[34:35]
	s_waitcnt vmcnt(8)
	s_waitcnt lgkmcnt(0)
	s_barrier
	s_setprio 1
	s_waitcnt lgkmcnt(0)
	v_mfma_f32_16x16x32_bf16 v[126:129], v[146:149], v[188:191], v[126:129]
	v_mfma_f32_16x16x32_bf16 v[122:125], v[162:165], v[188:191], v[122:125]
	v_mfma_f32_16x16x32_bf16 v[110:113], v[146:149], v[196:199], v[110:113]
	v_mfma_f32_16x16x32_bf16 v[106:109], v[162:165], v[196:199], v[106:109]
	v_mfma_f32_16x16x32_bf16 v[94:97], v[146:149], v[204:207], v[94:97]
	v_mfma_f32_16x16x32_bf16 v[90:93], v[162:165], v[204:207], v[90:93]
	v_mfma_f32_16x16x32_bf16 v[78:81], v[146:149], v[212:215], v[78:81]
	v_mfma_f32_16x16x32_bf16 v[74:77], v[162:165], v[212:215], v[74:77]
	v_mfma_f32_16x16x32_bf16 v[126:129], v[158:161], v[192:195], v[126:129]
	v_mfma_f32_16x16x32_bf16 v[122:125], v[166:169], v[192:195], v[122:125]
	v_mfma_f32_16x16x32_bf16 v[110:113], v[158:161], v[200:203], v[110:113]
	v_mfma_f32_16x16x32_bf16 v[106:109], v[166:169], v[200:203], v[106:109]
	v_mfma_f32_16x16x32_bf16 v[94:97], v[158:161], v[208:211], v[94:97]
	v_mfma_f32_16x16x32_bf16 v[90:93], v[166:169], v[208:211], v[90:93]
	v_mfma_f32_16x16x32_bf16 v[78:81], v[158:161], v[216:219], v[78:81]
	v_mfma_f32_16x16x32_bf16 v[74:77], v[166:169], v[216:219], v[74:77]
	s_setprio 0
	s_setprio 1
	v_mfma_f32_16x16x32_bf16 v[118:121], v[170:173], v[188:191], v[118:121]
	v_mfma_f32_16x16x32_bf16 v[114:117], v[178:181], v[188:191], v[114:117]
	v_mfma_f32_16x16x32_bf16 v[102:105], v[170:173], v[196:199], v[102:105]
	v_mfma_f32_16x16x32_bf16 v[98:101], v[178:181], v[196:199], v[98:101]
	v_mfma_f32_16x16x32_bf16 v[86:89], v[170:173], v[204:207], v[86:89]
	v_mfma_f32_16x16x32_bf16 v[82:85], v[178:181], v[204:207], v[82:85]
	v_mfma_f32_16x16x32_bf16 v[70:73], v[170:173], v[212:215], v[70:73]
	v_mfma_f32_16x16x32_bf16 v[66:69], v[178:181], v[212:215], v[66:69]
	v_mfma_f32_16x16x32_bf16 v[118:121], v[174:177], v[192:195], v[118:121]
	v_mfma_f32_16x16x32_bf16 v[114:117], v[184:187], v[192:195], v[114:117]
	v_mfma_f32_16x16x32_bf16 v[102:105], v[174:177], v[200:203], v[102:105]
	v_mfma_f32_16x16x32_bf16 v[98:101], v[184:187], v[200:203], v[98:101]
	v_mfma_f32_16x16x32_bf16 v[86:89], v[174:177], v[208:211], v[86:89]
	v_mfma_f32_16x16x32_bf16 v[82:85], v[184:187], v[208:211], v[82:85]
	v_mfma_f32_16x16x32_bf16 v[70:73], v[174:177], v[216:219], v[70:73]
	v_mfma_f32_16x16x32_bf16 v[66:69], v[184:187], v[216:219], v[66:69]
	s_setprio 0
	s_barrier
	s_add_i32 s34, s52, s36
	s_add_u32 s58, s30, s2
	s_addc_u32 s59, s31, s3
	s_mov_b32 m0, s34
	ds_read_b128 v[188:191], v156 offset:49152
	ds_read_b128 v[192:195], v156 offset:50176
	ds_read_b128 v[196:199], v156 offset:51200
	ds_read_b128 v[200:203], v156 offset:52224
	ds_read_b128 v[204:207], v156 offset:53248
	ds_read_b128 v[208:211], v156 offset:54272
	ds_read_b128 v[212:215], v156 offset:55296
	ds_read_b128 v[216:219], v156 offset:56320
	global_load_lds_dwordx4 v132, s[58:59]
	s_add_i32 m0, s34, 0x2000
	s_add_u32 s30, s30, 0x200080
	s_addc_u32 s31, s31, 0
	s_add_i32 s34, s53, s36
	global_load_lds_dwordx4 v136, s[58:59]
	s_mov_b32 m0, s34
	s_nop 0
	global_load_lds_dwordx4 v132, s[30:31]
	s_add_i32 m0, s34, 0x2000
	s_nop 0
	global_load_lds_dwordx4 v136, s[30:31]
	s_mov_b32 m0, s41
	s_nop 0
	global_load_lds_dwordx4 v130, s[60:61]
	s_mov_b32 m0, s42
	s_nop 0
	global_load_lds_dwordx4 v134, s[60:61]
	s_waitcnt vmcnt(8)
	s_waitcnt lgkmcnt(0)
	s_barrier
	s_setprio 1
	s_waitcnt lgkmcnt(0)
	v_mfma_f32_16x16x32_bf16 v[62:65], v[146:149], v[188:191], v[62:65]
	v_mfma_f32_16x16x32_bf16 v[58:61], v[162:165], v[188:191], v[58:61]
	v_mfma_f32_16x16x32_bf16 v[46:49], v[146:149], v[196:199], v[46:49]
	v_mfma_f32_16x16x32_bf16 v[42:45], v[162:165], v[196:199], v[42:45]
	v_mfma_f32_16x16x32_bf16 v[30:33], v[146:149], v[204:207], v[30:33]
	v_mfma_f32_16x16x32_bf16 v[26:29], v[162:165], v[204:207], v[26:29]
	v_mfma_f32_16x16x32_bf16 v[14:17], v[146:149], v[212:215], v[14:17]
	v_mfma_f32_16x16x32_bf16 v[10:13], v[162:165], v[212:215], v[10:13]
	v_mfma_f32_16x16x32_bf16 v[62:65], v[158:161], v[192:195], v[62:65]
	v_mfma_f32_16x16x32_bf16 v[58:61], v[166:169], v[192:195], v[58:61]
	v_mfma_f32_16x16x32_bf16 v[46:49], v[158:161], v[200:203], v[46:49]
	v_mfma_f32_16x16x32_bf16 v[42:45], v[166:169], v[200:203], v[42:45]
	v_mfma_f32_16x16x32_bf16 v[30:33], v[158:161], v[208:211], v[30:33]
	v_mfma_f32_16x16x32_bf16 v[26:29], v[166:169], v[208:211], v[26:29]
	v_mfma_f32_16x16x32_bf16 v[14:17], v[158:161], v[216:219], v[14:17]
	v_mfma_f32_16x16x32_bf16 v[10:13], v[166:169], v[216:219], v[10:13]
	s_setprio 0
	s_setprio 1
	v_mfma_f32_16x16x32_bf16 v[54:57], v[170:173], v[188:191], v[54:57]
	v_mfma_f32_16x16x32_bf16 v[50:53], v[178:181], v[188:191], v[50:53]
	v_mfma_f32_16x16x32_bf16 v[38:41], v[170:173], v[196:199], v[38:41]
	v_mfma_f32_16x16x32_bf16 v[34:37], v[178:181], v[196:199], v[34:37]
	v_mfma_f32_16x16x32_bf16 v[22:25], v[170:173], v[204:207], v[22:25]
	v_mfma_f32_16x16x32_bf16 v[18:21], v[178:181], v[204:207], v[18:21]
	v_mfma_f32_16x16x32_bf16 v[6:9], v[170:173], v[212:215], v[6:9]
	v_mfma_f32_16x16x32_bf16 v[2:5], v[178:181], v[212:215], v[2:5]
	v_mfma_f32_16x16x32_bf16 v[54:57], v[174:177], v[192:195], v[54:57]
	v_mfma_f32_16x16x32_bf16 v[50:53], v[184:187], v[192:195], v[50:53]
	v_mfma_f32_16x16x32_bf16 v[38:41], v[174:177], v[200:203], v[38:41]
	v_mfma_f32_16x16x32_bf16 v[34:37], v[184:187], v[200:203], v[34:37]
	v_mfma_f32_16x16x32_bf16 v[22:25], v[174:177], v[208:211], v[22:25]
	v_mfma_f32_16x16x32_bf16 v[18:21], v[184:187], v[208:211], v[18:21]
	v_mfma_f32_16x16x32_bf16 v[6:9], v[174:177], v[216:219], v[6:9]
	v_mfma_f32_16x16x32_bf16 v[2:5], v[184:187], v[216:219], v[2:5]
	s_setprio 0
	s_barrier
	s_add_i32 s51, s51, 2
	s_add_u32 s28, s28, 0x100
	s_addc_u32 s29, s29, 0
	s_add_u32 s49, s49, 0x100
	s_addc_u32 s50, s50, 0
	s_cmpk_gt_u32 s51, 0x7d
	s_cbranch_scc0 .LBB0_563
	s_and_b64 vcc, exec, s[8:9]
	s_cbranch_vccz .LBB0_566
	s_barrier

; #define PG8_STAGE(bufoff, gbase, voff) do { _Pragma("unroll") for (int _i = 0; _i < 2; ++_i) \
;         __builtin_amdgcn_global_load_lds((const unsigned*)((const char*)(gbase) + (voff)[_i]), (PG8_LAS unsigned*)(lds + (bufoff) + ldsw + _i * 8192), 16, 0, 0); } while (0)
; #define PG8_LDA(dst, b, h) do { _Pragma("unroll") for (int m = 0; m < 4; ++m) _Pragma("unroll") for (int k = 0; k < 2; ++k) dst[m][k] = *(const PG8_LAS bf16x8*)(lds + PG8_SA(b, h) + aoff + m * 2048 + k * 1024); } while (0)
; #define PG8_LDB(dst, b, h) do { _Pragma("unroll") for (int n = 0; n < 2; ++n) _Pragma("unroll") for (int k = 0; k < 2; ++k) dst[n][k] = *(const PG8_LAS bf16x8*)(lds + PG8_SB(b, h) + boff + n * 2048 + k * 1024); } while (0)
; #define PG8_MMA(ai, bj, At, Bt) do { __builtin_amdgcn_s_setprio(1); _Pragma("unroll") for (int m = 0; m < 4; ++m) _Pragma("unroll") for (int n = 0; n < 2; ++n) _Pragma("unroll") for (int k = 0; k < 2; ++k) \
;         acc[ai][bj][m][n] = __builtin_amdgcn_mfma_f32_16x16x32_bf16(Bt[n][k], At[m][k], acc[ai][bj][m][n], 0, 0, 0); __builtin_amdgcn_s_setprio(0); } while (0)
; #define PG8_WAIT_V(n) asm volatile("s_waitcnt vmcnt(" #n ")" ::: "memory")
; #define PG8_WAIT_L(n) asm volatile("s_waitcnt lgkmcnt(" #n ")" ::: "memory")
; template <class Epi, class Sched, bool ALIGN_EPI = false, bool SP2 = false>
; __device__ __forceinline__ void gemm_phase(PG8_LAS unsigned char* lds, const Gemm g, const Sched& S, const Epi& E) {
;     ...
;             const bool last = (t == nt - 2);
;             const char* a1 = cA + (size_t)(t + 1) * kstep;
;             const char* a2 = last ? nA : cA + (size_t)(t + 2) * kstep; const char* b2 = last ? nB : cB + (size_t)(t + 2) * kstep;
;             const char* a3 = a2 + kstep; const char* b3 = b2 + kstep;
;             if (last && has_next) S.a_ready(nxt);
;             if constexpr (SP2) {
;             PG8_LDB(B0, 0, 0); PG8_LDB(B1, 0, 1); PG8_SCHED; PG8_LDA(At, 0, 0); PG8_STAGE(PG8_SA(1, 1), a1 + hstep, voffA);
;             PG8_WAIT_V(8); PG8_WAIT_L(0); PG8_BAR; PG8_MMA(0, 0, At, B0); PG8_MMA(0, 1, At, B1); PG8_BAR; PG8_SCHED;
;             PG8_LDA(At, 0, 1); PG8_STAGE(PG8_SB(0, 0), b2, voffB); PG8_STAGE(PG8_SB(0, 1), b2 + hstep, voffB); PG8_STAGE(PG8_SA(0, 0), a2, voffA);
;             PG8_WAIT_V(8); PG8_WAIT_L(0); PG8_BAR; PG8_MMA(1, 0, At, B0); PG8_MMA(1, 1, At, B1); PG8_BAR; PG8_SCHED;
.LBB0_707:
	ds_read_b128 v[142:145], v151
	ds_read_b128 v[154:157], v151 offset:1024
	ds_read_b128 v[158:161], v151 offset:2048
	ds_read_b128 v[162:165], v151 offset:3072
	ds_read_b128 v[166:169], v152
	ds_read_b128 v[170:173], v152 offset:1024
	ds_read_b128 v[174:177], v152 offset:2048
	ds_read_b128 v[178:181], v152 offset:3072
	s_add_u32 s34, s30, 0xfff00080
	s_addc_u32 s35, s31, -1
	s_cmp_eq_u32 s61, 60
	s_cselect_b32 s37, s25, s35
	s_cselect_b32 s36, s57, s34
	s_cselect_b32 s35, s23, s60
	s_cselect_b32 s34, s58, s59
	s_add_i32 m0, s42, 0xc000
	ds_read_b128 v[184:187], v153
	ds_read_b128 v[188:191], v153 offset:1024
	ds_read_b128 v[192:195], v153 offset:2048
	ds_read_b128 v[196:199], v153 offset:3072
	ds_read_b128 v[200:203], v153 offset:4096
	ds_read_b128 v[204:207], v153 offset:5120
	ds_read_b128 v[208:211], v153 offset:6144
	ds_read_b128 v[212:215], v153 offset:7168
	global_load_lds_dwordx4 v134, s[30:31]
	s_add_i32 m0, s42, 0xe000
	s_nop 0
	global_load_lds_dwordx4 v136, s[30:31]
	s_waitcnt vmcnt(8)
	s_waitcnt lgkmcnt(0)
	s_barrier
	s_setprio 1
	s_waitcnt lgkmcnt(0)
	v_mfma_f32_16x16x32_bf16 v[126:129], v[142:145], v[184:187], v[126:129]
	v_mfma_f32_16x16x32_bf16 v[122:125], v[158:161], v[184:187], v[122:125]
	v_mfma_f32_16x16x32_bf16 v[110:113], v[142:145], v[192:195], v[110:113]
	v_mfma_f32_16x16x32_bf16 v[106:109], v[158:161], v[192:195], v[106:109]
	v_mfma_f32_16x16x32_bf16 v[94:97], v[142:145], v[200:203], v[94:97]
	v_mfma_f32_16x16x32_bf16 v[90:93], v[158:161], v[200:203], v[90:93]
	v_mfma_f32_16x16x32_bf16 v[86:89], v[142:145], v[208:211], v[86:89]
	v_mfma_f32_16x16x32_bf16 v[78:81], v[158:161], v[208:211], v[78:81]
	v_mfma_f32_16x16x32_bf16 v[126:129], v[154:157], v[188:191], v[126:129]
	v_mfma_f32_16x16x32_bf16 v[122:125], v[162:165], v[188:191], v[122:125]
	v_mfma_f32_16x16x32_bf16 v[110:113], v[154:157], v[196:199], v[110:113]
	v_mfma_f32_16x16x32_bf16 v[106:109], v[162:165], v[196:199], v[106:109]
	v_mfma_f32_16x16x32_bf16 v[94:97], v[154:157], v[204:207], v[94:97]
	v_mfma_f32_16x16x32_bf16 v[90:93], v[162:165], v[204:207], v[90:93]
	v_mfma_f32_16x16x32_bf16 v[86:89], v[154:157], v[212:215], v[86:89]
	v_mfma_f32_16x16x32_bf16 v[78:81], v[162:165], v[212:215], v[78:81]
	s_setprio 0
	s_setprio 1
	v_mfma_f32_16x16x32_bf16 v[118:121], v[166:169], v[184:187], v[118:121]
	v_mfma_f32_16x16x32_bf16 v[114:117], v[174:177], v[184:187], v[114:117]
	v_mfma_f32_16x16x32_bf16 v[102:105], v[166:169], v[192:195], v[102:105]
	v_mfma_f32_16x16x32_bf16 v[98:101], v[174:177], v[192:195], v[98:101]
	v_mfma_f32_16x16x32_bf16 v[82:85], v[166:169], v[200:203], v[82:85]
	v_mfma_f32_16x16x32_bf16 v[74:77], v[174:177], v[200:203], v[74:77]
	v_mfma_f32_16x16x32_bf16 v[70:73], v[166:169], v[208:211], v[70:73]
	v_mfma_f32_16x16x32_bf16 v[66:69], v[174:177], v[208:211], v[66:69]
	v_mfma_f32_16x16x32_bf16 v[118:121], v[170:173], v[188:191], v[118:121]
	v_mfma_f32_16x16x32_bf16 v[114:117], v[178:181], v[188:191], v[114:117]
	v_mfma_f32_16x16x32_bf16 v[102:105], v[170:173], v[196:199], v[102:105]
	v_mfma_f32_16x16x32_bf16 v[98:101], v[178:181], v[196:199], v[98:101]
	v_mfma_f32_16x16x32_bf16 v[82:85], v[170:173], v[204:207], v[82:85]
	v_mfma_f32_16x16x32_bf16 v[74:77], v[178:181], v[204:207], v[74:77]
	v_mfma_f32_16x16x32_bf16 v[70:73], v[170:173], v[212:215], v[70:73]
	v_mfma_f32_16x16x32_bf16 v[66:69], v[178:181], v[212:215], v[66:69]
	s_setprio 0
	s_barrier
	s_add_i32 s62, s51, s33
	s_mov_b32 m0, s62
	ds_read_b128 v[184:187], v153 offset:16384
	ds_read_b128 v[188:191], v153 offset:17408
	ds_read_b128 v[192:195], v153 offset:18432
	ds_read_b128 v[196:199], v153 offset:19456
	ds_read_b128 v[200:203], v153 offset:20480
	ds_read_b128 v[204:207], v153 offset:21504
	ds_read_b128 v[208:211], v153 offset:22528
	ds_read_b128 v[212:215], v153 offset:23552
	global_load_lds_dwordx4 v130, s[34:35]
	s_add_i32 m0, s62, 0x2000
	s_add_u32 s62, s34, 0x100000
	s_addc_u32 s63, s35, 0
	s_add_i32 s72, s52, s33
	global_load_lds_dwordx4 v132, s[34:35]
	s_mov_b32 m0, s72
	s_add_u32 s84, s36, s12
	s_addc_u32 s85, s37, s13
	global_load_lds_dwordx4 v130, s[62:63]
	s_add_i32 m0, s72, 0x2000
	s_nop 0
	global_load_lds_dwordx4 v132, s[62:63]
	s_mov_b32 m0, s42
	s_nop 0
	global_load_lds_dwordx4 v130, s[36:37]
	s_mov_b32 m0, s43
	s_nop 0
	global_load_lds_dwordx4 v132, s[36:37]
	s_waitcnt vmcnt(8)
	s_waitcnt lgkmcnt(0)
	s_barrier
	s_setprio 1
	s_waitcnt lgkmcnt(0)
	v_mfma_f32_16x16x32_bf16 v[62:65], v[142:145], v[184:187], v[62:65]
	v_mfma_f32_16x16x32_bf16 v[58:61], v[158:161], v[184:187], v[58:61]
	v_mfma_f32_16x16x32_bf16 v[50:53], v[142:145], v[192:195], v[50:53]
	v_mfma_f32_16x16x32_bf16 v[42:45], v[158:161], v[192:195], v[42:45]
	v_mfma_f32_16x16x32_bf16 v[34:37], v[142:145], v[200:203], v[34:37]
	v_mfma_f32_16x16x32_bf16 v[26:29], v[158:161], v[200:203], v[26:29]
	v_mfma_f32_16x16x32_bf16 v[14:17], v[142:145], v[208:211], v[14:17]
	v_mfma_f32_16x16x32_bf16 v[10:13], v[158:161], v[208:211], v[10:13]
	v_mfma_f32_16x16x32_bf16 v[62:65], v[154:157], v[188:191], v[62:65]
	v_mfma_f32_16x16x32_bf16 v[58:61], v[162:165], v[188:191], v[58:61]
	v_mfma_f32_16x16x32_bf16 v[50:53], v[154:157], v[196:199], v[50:53]
	v_mfma_f32_16x16x32_bf16 v[42:45], v[162:165], v[196:199], v[42:45]
	v_mfma_f32_16x16x32_bf16 v[34:37], v[154:157], v[204:207], v[34:37]
	v_mfma_f32_16x16x32_bf16 v[26:29], v[162:165], v[204:207], v[26:29]
	v_mfma_f32_16x16x32_bf16 v[14:17], v[154:157], v[212:215], v[14:17]
	v_mfma_f32_16x16x32_bf16 v[10:13], v[162:165], v[212:215], v[10:13]
	s_setprio 0
	s_setprio 1
	v_mfma_f32_16x16x32_bf16 v[54:57], v[166:169], v[184:187], v[54:57]
	v_mfma_f32_16x16x32_bf16 v[46:49], v[174:177], v[184:187], v[46:49]
	v_mfma_f32_16x16x32_bf16 v[38:41], v[166:169], v[192:195], v[38:41]
	v_mfma_f32_16x16x32_bf16 v[30:33], v[174:177], v[192:195], v[30:33]
	v_mfma_f32_16x16x32_bf16 v[22:25], v[166:169], v[200:203], v[22:25]
	v_mfma_f32_16x16x32_bf16 v[18:21], v[174:177], v[200:203], v[18:21]
	v_mfma_f32_16x16x32_bf16 v[6:9], v[166:169], v[208:211], v[6:9]
	v_mfma_f32_16x16x32_bf16 v[2:5], v[174:177], v[208:211], v[2:5]
	v_mfma_f32_16x16x32_bf16 v[54:57], v[170:173], v[188:191], v[54:57]
	v_mfma_f32_16x16x32_bf16 v[46:49], v[178:181], v[188:191], v[46:49]
	v_mfma_f32_16x16x32_bf16 v[38:41], v[170:173], v[196:199], v[38:41]
	v_mfma_f32_16x16x32_bf16 v[30:33], v[178:181], v[196:199], v[30:33]
	v_mfma_f32_16x16x32_bf16 v[22:25], v[170:173], v[204:207], v[22:25]
	v_mfma_f32_16x16x32_bf16 v[18:21], v[178:181], v[204:207], v[18:21]
	v_mfma_f32_16x16x32_bf16 v[6:9], v[170:173], v[212:215], v[6:9]
	v_mfma_f32_16x16x32_bf16 v[2:5], v[178:181], v[212:215], v[2:5]
	s_setprio 0
	s_barrier
; #define PG8_STAGE(bufoff, gbase, voff) do { _Pragma("unroll") for (int _i = 0; _i < 2; ++_i) \
;         __builtin_amdgcn_global_load_lds((const unsigned*)((const char*)(gbase) + (voff)[_i]), (PG8_LAS unsigned*)(lds + (bufoff) + ldsw + _i * 8192), 16, 0, 0); } while (0)
; #define PG8_LDA(dst, b, h) do { _Pragma("unroll") for (int m = 0; m < 4; ++m) _Pragma("unroll") for (int k = 0; k < 2; ++k) dst[m][k] = *(const PG8_LAS bf16x8*)(lds + PG8_SA(b, h) + aoff + m * 2048 + k * 1024); } while (0)
; #define PG8_LDB(dst, b, h) do { _Pragma("unroll") for (int n = 0; n < 2; ++n) _Pragma("unroll") for (int k = 0; k < 2; ++k) dst[n][k] = *(const PG8_LAS bf16x8*)(lds + PG8_SB(b, h) + boff + n * 2048 + k * 1024); } while (0)
; #define PG8_MMA(ai, bj, At, Bt) do { __builtin_amdgcn_s_setprio(1); _Pragma("unroll") for (int m = 0; m < 4; ++m) _Pragma("unroll") for (int n = 0; n < 2; ++n) _Pragma("unroll") for (int k = 0; k < 2; ++k) \
;         acc[ai][bj][m][n] = __builtin_amdgcn_mfma_f32_16x16x32_bf16(Bt[n][k], At[m][k], acc[ai][bj][m][n], 0, 0, 0); __builtin_amdgcn_s_setprio(0); } while (0)
; #define PG8_WAIT_V(n) asm volatile("s_waitcnt vmcnt(" #n ")" ::: "memory")
; #define PG8_WAIT_L(n) asm volatile("s_waitcnt lgkmcnt(" #n ")" ::: "memory")
; #define PG8_BAR __builtin_amdgcn_s_barrier()
; #define PG8_SCHED __builtin_amdgcn_sched_barrier(0)
; template <class Epi, class Sched, bool ALIGN_EPI = false, bool SP2 = false>
; __device__ __forceinline__ void gemm_phase(PG8_LAS unsigned char* lds, const Gemm g, const Sched& S, const Epi& E) {
;     ...
;             PG8_LDB(B0, 1, 0); PG8_LDB(B1, 1, 1); PG8_SCHED; PG8_LDA(At, 1, 0); PG8_STAGE(PG8_SA(0, 1), a2 + hstep, voffA);
;             PG8_WAIT_V(8); PG8_WAIT_L(0); PG8_BAR; PG8_MMA(0, 0, At, B0); PG8_MMA(0, 1, At, B1); PG8_BAR; PG8_SCHED;
;             PG8_LDA(At, 1, 1); PG8_STAGE(PG8_SB(1, 0), b3, voffB); PG8_STAGE(PG8_SB(1, 1), b3 + hstep, voffB); PG8_STAGE(PG8_SA(1, 0), a3, voffA);
;             PG8_WAIT_V(8); PG8_WAIT_L(0); PG8_BAR; PG8_MMA(1, 0, At, B0); PG8_MMA(1, 1, At, B1); PG8_BAR; PG8_SCHED;
;     ...
;         if constexpr (ALIGN_EPI) { if (wr == 0) PG8_BAR; }
	s_add_i32 s62, 0, 0x18000
	s_add_i32 s63, 0, 0x1c000
	v_add_u32_e32 v162, s62, v149
	v_add_u32_e32 v178, s63, v149
	ds_read_b128 v[142:145], v162
	ds_read_b128 v[154:157], v162 offset:1024
	ds_read_b128 v[158:161], v162 offset:2048
	ds_read_b128 v[162:165], v162 offset:3072
	ds_read_b128 v[166:169], v178
	ds_read_b128 v[170:173], v178 offset:1024
	ds_read_b128 v[174:177], v178 offset:2048
	ds_read_b128 v[178:181], v178 offset:3072
	s_add_u32 s36, s36, 0x100000
	s_addc_u32 s37, s37, 0
	s_mov_b32 m0, s44
	ds_read_b128 v[184:187], v153 offset:32768
	ds_read_b128 v[188:191], v153 offset:33792
	ds_read_b128 v[192:195], v153 offset:34816
	ds_read_b128 v[196:199], v153 offset:35840
	ds_read_b128 v[200:203], v153 offset:36864
	ds_read_b128 v[204:207], v153 offset:37888
	ds_read_b128 v[208:211], v153 offset:38912
	ds_read_b128 v[212:215], v153 offset:39936
	global_load_lds_dwordx4 v130, s[36:37]
	s_mov_b32 m0, s45
	s_nop 0
	global_load_lds_dwordx4 v132, s[36:37]
	s_waitcnt vmcnt(8)
	s_waitcnt lgkmcnt(0)
	s_barrier
	s_setprio 1
	s_waitcnt lgkmcnt(0)
	v_mfma_f32_16x16x32_bf16 v[126:129], v[142:145], v[184:187], v[126:129]
	v_mfma_f32_16x16x32_bf16 v[122:125], v[158:161], v[184:187], v[122:125]
	v_mfma_f32_16x16x32_bf16 v[110:113], v[142:145], v[192:195], v[110:113]
	v_mfma_f32_16x16x32_bf16 v[106:109], v[158:161], v[192:195], v[106:109]
	v_mfma_f32_16x16x32_bf16 v[94:97], v[142:145], v[200:203], v[94:97]
	v_mfma_f32_16x16x32_bf16 v[90:93], v[158:161], v[200:203], v[90:93]
	v_mfma_f32_16x16x32_bf16 v[86:89], v[142:145], v[208:211], v[86:89]
	v_mfma_f32_16x16x32_bf16 v[78:81], v[158:161], v[208:211], v[78:81]
	v_mfma_f32_16x16x32_bf16 v[126:129], v[154:157], v[188:191], v[126:129]
	v_mfma_f32_16x16x32_bf16 v[122:125], v[162:165], v[188:191], v[122:125]
	v_mfma_f32_16x16x32_bf16 v[110:113], v[154:157], v[196:199], v[110:113]
	v_mfma_f32_16x16x32_bf16 v[106:109], v[162:165], v[196:199], v[106:109]
	v_mfma_f32_16x16x32_bf16 v[94:97], v[154:157], v[204:207], v[94:97]
	v_mfma_f32_16x16x32_bf16 v[90:93], v[162:165], v[204:207], v[90:93]
	v_mfma_f32_16x16x32_bf16 v[86:89], v[154:157], v[212:215], v[86:89]
	v_mfma_f32_16x16x32_bf16 v[78:81], v[162:165], v[212:215], v[78:81]
	s_setprio 0
	s_setprio 1
	v_mfma_f32_16x16x32_bf16 v[118:121], v[166:169], v[184:187], v[118:121]
	v_mfma_f32_16x16x32_bf16 v[114:117], v[174:177], v[184:187], v[114:117]
	v_mfma_f32_16x16x32_bf16 v[102:105], v[166:169], v[192:195], v[102:105]
	v_mfma_f32_16x16x32_bf16 v[98:101], v[174:177], v[192:195], v[98:101]
	v_mfma_f32_16x16x32_bf16 v[82:85], v[166:169], v[200:203], v[82:85]
	v_mfma_f32_16x16x32_bf16 v[74:77], v[174:177], v[200:203], v[74:77]
	v_mfma_f32_16x16x32_bf16 v[70:73], v[166:169], v[208:211], v[70:73]
	v_mfma_f32_16x16x32_bf16 v[66:69], v[174:177], v[208:211], v[66:69]
	v_mfma_f32_16x16x32_bf16 v[118:121], v[170:173], v[188:191], v[118:121]
	v_mfma_f32_16x16x32_bf16 v[114:117], v[178:181], v[188:191], v[114:117]
	v_mfma_f32_16x16x32_bf16 v[102:105], v[170:173], v[196:199], v[102:105]
	v_mfma_f32_16x16x32_bf16 v[98:101], v[178:181], v[196:199], v[98:101]
	v_mfma_f32_16x16x32_bf16 v[82:85], v[170:173], v[204:207], v[82:85]
	v_mfma_f32_16x16x32_bf16 v[74:77], v[178:181], v[204:207], v[74:77]
	v_mfma_f32_16x16x32_bf16 v[70:73], v[170:173], v[212:215], v[70:73]
	v_mfma_f32_16x16x32_bf16 v[66:69], v[178:181], v[212:215], v[66:69]
	s_setprio 0
	s_barrier
	s_add_i32 s36, s62, s33
	s_add_u32 s82, s34, s12
	s_addc_u32 s83, s35, s13
	s_mov_b32 m0, s36
	ds_read_b128 v[184:187], v153 offset:49152
	ds_read_b128 v[188:191], v153 offset:50176
	ds_read_b128 v[192:195], v153 offset:51200
	ds_read_b128 v[196:199], v153 offset:52224
	ds_read_b128 v[200:203], v153 offset:53248
	ds_read_b128 v[204:207], v153 offset:54272
	ds_read_b128 v[208:211], v153 offset:55296
	ds_read_b128 v[212:215], v153 offset:56320
	global_load_lds_dwordx4 v130, s[82:83]
	s_add_i32 m0, s36, 0x2000
	s_add_u32 s34, s34, 0x100080
	s_addc_u32 s35, s35, 0
	s_add_i32 s36, s63, s33
	global_load_lds_dwordx4 v132, s[82:83]
	s_mov_b32 m0, s36
	s_nop 0
	global_load_lds_dwordx4 v130, s[34:35]
	s_add_i32 m0, s36, 0x2000
	s_nop 0
	global_load_lds_dwordx4 v132, s[34:35]
	s_mov_b32 m0, s49
	s_nop 0
	global_load_lds_dwordx4 v130, s[84:85]
	s_mov_b32 m0, s50
	s_nop 0
	global_load_lds_dwordx4 v132, s[84:85]
	s_waitcnt vmcnt(8)
	s_waitcnt lgkmcnt(0)
	s_barrier
	s_setprio 1
	s_waitcnt lgkmcnt(0)
	v_mfma_f32_16x16x32_bf16 v[62:65], v[142:145], v[184:187], v[62:65]
	v_mfma_f32_16x16x32_bf16 v[58:61], v[158:161], v[184:187], v[58:61]
	v_mfma_f32_16x16x32_bf16 v[50:53], v[142:145], v[192:195], v[50:53]
	v_mfma_f32_16x16x32_bf16 v[42:45], v[158:161], v[192:195], v[42:45]
	v_mfma_f32_16x16x32_bf16 v[34:37], v[142:145], v[200:203], v[34:37]
	v_mfma_f32_16x16x32_bf16 v[26:29], v[158:161], v[200:203], v[26:29]
	v_mfma_f32_16x16x32_bf16 v[14:17], v[142:145], v[208:211], v[14:17]
	v_mfma_f32_16x16x32_bf16 v[10:13], v[158:161], v[208:211], v[10:13]
	v_mfma_f32_16x16x32_bf16 v[62:65], v[154:157], v[188:191], v[62:65]
	v_mfma_f32_16x16x32_bf16 v[58:61], v[162:165], v[188:191], v[58:61]
	v_mfma_f32_16x16x32_bf16 v[50:53], v[154:157], v[196:199], v[50:53]
	v_mfma_f32_16x16x32_bf16 v[42:45], v[162:165], v[196:199], v[42:45]
	v_mfma_f32_16x16x32_bf16 v[34:37], v[154:157], v[204:207], v[34:37]
	v_mfma_f32_16x16x32_bf16 v[26:29], v[162:165], v[204:207], v[26:29]
	v_mfma_f32_16x16x32_bf16 v[14:17], v[154:157], v[212:215], v[14:17]
	v_mfma_f32_16x16x32_bf16 v[10:13], v[162:165], v[212:215], v[10:13]
	s_setprio 0
	s_setprio 1
	v_mfma_f32_16x16x32_bf16 v[54:57], v[166:169], v[184:187], v[54:57]
	v_mfma_f32_16x16x32_bf16 v[46:49], v[174:177], v[184:187], v[46:49]
	v_mfma_f32_16x16x32_bf16 v[38:41], v[166:169], v[192:195], v[38:41]
	v_mfma_f32_16x16x32_bf16 v[30:33], v[174:177], v[192:195], v[30:33]
	v_mfma_f32_16x16x32_bf16 v[22:25], v[166:169], v[200:203], v[22:25]
	v_mfma_f32_16x16x32_bf16 v[18:21], v[174:177], v[200:203], v[18:21]
	v_mfma_f32_16x16x32_bf16 v[6:9], v[166:169], v[208:211], v[6:9]
	v_mfma_f32_16x16x32_bf16 v[2:5], v[174:177], v[208:211], v[2:5]
	v_mfma_f32_16x16x32_bf16 v[54:57], v[170:173], v[188:191], v[54:57]
	v_mfma_f32_16x16x32_bf16 v[46:49], v[178:181], v[188:191], v[46:49]
	v_mfma_f32_16x16x32_bf16 v[38:41], v[170:173], v[196:199], v[38:41]
	v_mfma_f32_16x16x32_bf16 v[30:33], v[178:181], v[196:199], v[30:33]
	v_mfma_f32_16x16x32_bf16 v[22:25], v[170:173], v[204:207], v[22:25]
	v_mfma_f32_16x16x32_bf16 v[18:21], v[178:181], v[204:207], v[18:21]
	v_mfma_f32_16x16x32_bf16 v[6:9], v[170:173], v[212:215], v[6:9]
	v_mfma_f32_16x16x32_bf16 v[2:5], v[178:181], v[212:215], v[2:5]
	s_setprio 0
	s_barrier
	s_add_i32 s61, s61, 2
	s_add_u32 s30, s30, 0x100
	s_addc_u32 s31, s31, 0
	s_add_u32 s59, s59, 0x100
	s_addc_u32 s60, s60, 0
	s_cmp_gt_u32 s61, 61
	s_cbranch_scc0 .LBB0_707
	s_and_b64 vcc, exec, s[14:15]
	s_cbranch_vccz .LBB0_710
	s_barrier
